# baseline (speedup 1.0000x reference)
_Z11gemm_kernelILi2EEvPKDF16_S1_PKfPDF16_PfS5_S3_S3_S1_S3_:
	s_load_dwordx4 s[8:11], s[0:1], 0x28
	s_load_dwordx4 s[4:7], s[0:1], 0x0
	v_mov_b32_e32 v211, 0
	v_lshlrev_b32_e32 v178, 2, v0
	v_mov_b32_e32 v179, v211
	s_waitcnt lgkmcnt(0)
	v_lshl_add_u64 v[2:3], s[8:9], 0, v[178:179]
	s_movk_i32 s3, 0x1000
	v_add_co_u32_e32 v4, vcc, s3, v2
	s_movk_i32 s14, 0x2000
	s_nop 0
	v_addc_co_u32_e32 v5, vcc, 0, v3, vcc
	v_add_co_u32_e32 v6, vcc, s14, v2
	s_movk_i32 s15, 0x3000
	s_nop 0
	v_addc_co_u32_e32 v7, vcc, 0, v3, vcc
	global_load_dword v36, v178, s[8:9]
	global_load_dword v37, v178, s[8:9] offset:1024
	global_load_dword v38, v178, s[8:9] offset:2048
	global_load_dword v39, v178, s[8:9] offset:3072
	global_load_dword v40, v[6:7], off offset:-4096
	global_load_dword v41, v[4:5], off offset:1024
	global_load_dword v44, v[4:5], off offset:2048
	global_load_dword v45, v[4:5], off offset:3072
	global_load_dword v46, v[6:7], off
	global_load_dword v47, v[6:7], off offset:1024
	global_load_dword v48, v[6:7], off offset:2048
	global_load_dword v49, v[6:7], off offset:3072
	v_add_co_u32_e32 v2, vcc, s15, v2
	v_lshrrev_b32_e32 v1, 6, v0
	s_nop 0
	v_addc_co_u32_e32 v3, vcc, 0, v3, vcc
	global_load_dword v50, v[2:3], off
	global_load_dword v51, v[2:3], off offset:1024
	global_load_dword v52, v[2:3], off offset:2048
	global_load_dword v53, v[2:3], off offset:3072
	s_load_dwordx2 s[8:9], s[0:1], 0x48
	s_load_dwordx2 s[12:13], s[0:1], 0x38
	global_load_dword v54, v178, s[10:11]
	s_waitcnt lgkmcnt(0)
	global_load_dword v112, v178, s[8:9]
	global_load_dword v120, v178, s[12:13]
	v_lshlrev_b32_e32 v2, 4, v0
	v_and_b32_e32 v2, 0x3f0, v2
	v_lshl_or_b32 v210, v1, 15, v2
	v_lshl_add_u64 v[94:95], s[6:7], 0, v[210:211]
	v_add_co_u32_e32 v42, vcc, s3, v94
	s_movk_i32 s9, 0x4000
	s_nop 0
	v_addc_co_u32_e32 v43, vcc, 0, v95, vcc
	v_add_co_u32_e32 v34, vcc, s14, v94
	s_mov_b32 s8, 0x800000
	s_nop 0
	v_addc_co_u32_e32 v35, vcc, 0, v95, vcc
	v_add_co_u32_e32 v66, vcc, s15, v94
	s_movk_i32 s3, 0x5000
	s_nop 0
	v_addc_co_u32_e32 v67, vcc, 0, v95, vcc
	v_add_co_u32_e32 v68, vcc, s9, v94
	v_lshrrev_b32_e32 v180, 5, v0
	s_nop 0
	v_addc_co_u32_e32 v69, vcc, 0, v95, vcc
	s_lshl_b32 s16, s2, 5
	v_lshrrev_b32_e32 v160, 5, v0
	v_and_b32_e32 v161, 31, v0
	v_or_b32_e32 v160, s16, v160
	v_lshlrev_b32_e32 v161, 4, v161
	v_min_i32_e32 v146, 0xc34f, v160
	v_or_b32_e32 v150, 8, v160
	v_or_b32_e32 v154, 16, v160
	v_or_b32_e32 v158, 24, v160
	v_min_i32_e32 v150, 0xc34f, v150
	v_min_i32_e32 v154, 0xc34f, v154
	v_min_i32_e32 v158, 0xc34f, v158
	v_lshl_add_u32 v146, v146, 9, v161
	v_lshl_add_u32 v150, v150, 9, v161
	v_lshl_add_u32 v154, v154, 9, v161
	v_lshl_add_u32 v158, v158, 9, v161
	global_load_dwordx4 v[146:149], v146, s[4:5] nt
	global_load_dwordx4 v[150:153], v150, s[4:5] nt
	global_load_dwordx4 v[154:157], v154, s[4:5] nt
	global_load_dwordx4 v[158:161], v158, s[4:5] nt
	global_load_dwordx4 v[2:5], v[42:43], off offset:1024
	global_load_dwordx4 v[6:9], v[42:43], off offset:2048
	global_load_dwordx4 v[10:13], v[34:35], off offset:-4096
	global_load_dwordx4 v[14:17], v[34:35], off
	global_load_dwordx4 v[18:21], v[34:35], off offset:1024
	global_load_dwordx4 v[22:25], v[34:35], off offset:2048
	global_load_dwordx4 v[26:29], v[34:35], off offset:3072
	global_load_dwordx4 v[30:33], v[68:69], off offset:-4096
	v_and_b32_e32 v179, 31, v0
	v_lshlrev_b32_e32 v142, 5, v179
	s_waitcnt vmcnt(30)
	v_add_f32_e32 v34, 0, v36
	s_waitcnt vmcnt(29)
	v_add_f32_e32 v35, 0, v37
	s_waitcnt vmcnt(28)
	v_add_f32_e32 v34, v34, v38
	s_waitcnt vmcnt(27)
	v_add_f32_e32 v35, v35, v39
	s_waitcnt vmcnt(26)
	v_add_f32_e32 v34, v34, v40
	s_waitcnt vmcnt(25)
	v_add_f32_e32 v35, v35, v41
	s_waitcnt vmcnt(24)
	v_add_f32_e32 v34, v34, v44
	s_waitcnt vmcnt(23)
	v_add_f32_e32 v35, v35, v45
	s_waitcnt vmcnt(22)
	v_add_f32_e32 v34, v34, v46
	s_waitcnt vmcnt(21)
	v_add_f32_e32 v35, v35, v47
	s_waitcnt vmcnt(20)
	v_add_f32_e32 v34, v34, v48
	s_waitcnt vmcnt(19)
	v_add_f32_e32 v35, v35, v49
	s_waitcnt vmcnt(18)
	v_add_f32_e32 v34, v34, v50
	s_waitcnt vmcnt(17)
	v_add_f32_e32 v35, v35, v51
	s_waitcnt vmcnt(16)
	v_add_f32_e32 v44, v34, v52
	s_waitcnt vmcnt(15)
	v_add_f32_e32 v34, v35, v53
	v_mul_f32_e32 v35, 0x37a7c5ac, v44
	v_mul_f32_e32 v34, 0x37a7c5ac, v34
	v_fma_f32 v34, -v35, v35, v34
	v_add_f32_e32 v34, 0x3727c5ac, v34
	v_mul_f32_e32 v35, 0x4b800000, v34
	v_cmp_gt_f32_e32 vcc, s8, v34
	s_waitcnt vmcnt(13)
	v_fmamk_f32 v113, v44, 0x37a7c5ac, v112
	v_cndmask_b32_e32 v34, v34, v35, vcc
	v_rsq_f32_e32 v45, v34
	global_load_dwordx4 v[34:37], v[42:43], off offset:3072
	global_load_dwordx4 v[38:41], v[66:67], off offset:1024
	v_mul_f32_e32 v42, 0x45800000, v45
	v_cndmask_b32_e32 v42, v45, v42, vcc
	v_add_co_u32_e32 v110, vcc, s3, v94
	s_movk_i32 s3, 0x6000
	s_nop 0
	v_addc_co_u32_e32 v111, vcc, 0, v95, vcc
	v_add_co_u32_e32 v96, vcc, s3, v94
	s_movk_i32 s3, 0x7000
	s_nop 0
	v_addc_co_u32_e32 v97, vcc, 0, v95, vcc
	v_add_co_u32_e32 v118, vcc, s3, v94
	v_mul_f32_e32 v121, v42, v54
	global_load_dwordx4 v[42:45], v[66:67], off offset:2048
	global_load_dwordx4 v[46:49], v[66:67], off offset:3072
	global_load_dwordx4 v[50:53], v[68:69], off
	global_load_dwordx4 v[54:57], v[68:69], off offset:1024
	global_load_dwordx4 v[58:61], v[68:69], off offset:2048
	global_load_dwordx4 v[62:65], v[68:69], off offset:3072
	s_nop 0
	global_load_dwordx4 v[66:69], v[110:111], off offset:1024
	global_load_dwordx4 v[70:73], v[110:111], off offset:2048
	global_load_dwordx4 v[74:77], v[96:97], off offset:-4096
	global_load_dwordx4 v[78:81], v[96:97], off
	global_load_dwordx4 v[82:85], v[96:97], off offset:1024
	global_load_dwordx4 v[86:89], v[96:97], off offset:2048
	global_load_dwordx4 v[90:93], v[96:97], off offset:3072
	v_addc_co_u32_e32 v119, vcc, 0, v95, vcc
	global_load_dwordx4 v[94:97], v[110:111], off offset:3072
	global_load_dwordx4 v[98:101], v[118:119], off
	global_load_dwordx4 v[102:105], v[118:119], off offset:1024
	global_load_dwordx4 v[106:109], v[118:119], off offset:2048
	v_sub_f32_e32 v110, v112, v113
	s_waitcnt vmcnt(31)
	v_fmac_f32_e32 v120, v110, v121
	global_load_dwordx4 v[110:113], v210, s[6:7]
	global_load_dwordx4 v[114:117], v[118:119], off offset:3072
	ds_write2st64_b32 v178, v121, v120 offset1:4
	global_load_dwordx4 v[118:121], v210, s[6:7] offset:1024
	global_load_dwordx4 v[122:125], v210, s[6:7] offset:2048
	global_load_dwordx4 v[126:129], v210, s[6:7] offset:3072
	s_lshl_b32 s6, s2, 5
	v_lshlrev_b32_e32 v210, 4, v179
	s_waitcnt lgkmcnt(0)
	s_barrier
	ds_read_b128 v[130:133], v142
	ds_read_b128 v[134:137], v142 offset:16
	ds_read_b128 v[138:141], v142 offset:1024
	ds_read_b128 v[142:145], v142 offset:1040
	s_waitcnt lgkmcnt(0)
	s_barrier
	s_movk_i32 s7, 0x210
	v_mad_u32_u24 v216, v180, s7, v210
	s_mov_b32 s3, 0
	s_cmpk_gt_i32 s2, 0x61a
	s_waitcnt vmcnt(35)
	v_cvt_f32_f16_e32 v162, v146
	v_cvt_f32_f16_sdwa v163, v146 dst_sel:DWORD dst_unused:UNUSED_PAD src0_sel:WORD_1
	v_cvt_f32_f16_e32 v164, v147
	v_cvt_f32_f16_sdwa v165, v147 dst_sel:DWORD dst_unused:UNUSED_PAD src0_sel:WORD_1
	v_pk_fma_f32 v[162:163], v[130:131], v[162:163], v[138:139]
	s_nop 0
	v_max_f32_e32 v166, 0, v163
	v_max_f32_e32 v167, 0, v162
	v_pk_fma_f32 v[162:163], v[132:133], v[164:165], v[140:141]
	v_cvt_f32_f16_e32 v164, v148
	v_cvt_f32_f16_sdwa v165, v148 dst_sel:DWORD dst_unused:UNUSED_PAD src0_sel:WORD_1
	v_max_f32_e32 v168, 0, v162
	v_cvt_pk_f16_f32 v162, v167, v166
	v_cvt_f32_f16_e32 v166, v149
	v_cvt_f32_f16_sdwa v167, v149 dst_sel:DWORD dst_unused:UNUSED_PAD src0_sel:WORD_1
	v_pk_fma_f32 v[164:165], v[134:135], v[164:165], v[142:143]
	v_max_f32_e32 v163, 0, v163
	v_max_f32_e32 v165, 0, v165
	v_max_f32_e32 v164, 0, v164
	v_pk_fma_f32 v[166:167], v[136:137], v[166:167], v[144:145]
	v_cvt_pk_f16_f32 v164, v164, v165
	v_max_f32_e32 v165, 0, v167
	v_max_f32_e32 v166, 0, v166
	v_cvt_pk_f16_f32 v163, v168, v163
	v_cvt_pk_f16_f32 v165, v166, v165
	s_waitcnt vmcnt(34)
	v_cvt_f32_f16_e32 v166, v150
	v_cvt_f32_f16_sdwa v167, v150 dst_sel:DWORD dst_unused:UNUSED_PAD src0_sel:WORD_1
	ds_write_b128 v216, v[162:165]
	v_cvt_f32_f16_e32 v162, v151
	v_cvt_f32_f16_sdwa v163, v151 dst_sel:DWORD dst_unused:UNUSED_PAD src0_sel:WORD_1
	v_pk_fma_f32 v[164:165], v[130:131], v[166:167], v[138:139]
	v_pk_fma_f32 v[162:163], v[132:133], v[162:163], v[140:141]
	v_max_f32_e32 v166, 0, v165
	v_max_f32_e32 v167, 0, v164
	v_cvt_f32_f16_e32 v164, v152
	v_cvt_f32_f16_sdwa v165, v152 dst_sel:DWORD dst_unused:UNUSED_PAD src0_sel:WORD_1
	v_max_f32_e32 v168, 0, v162
	v_cvt_pk_f16_f32 v162, v167, v166
	v_cvt_f32_f16_e32 v166, v153
	v_cvt_f32_f16_sdwa v167, v153 dst_sel:DWORD dst_unused:UNUSED_PAD src0_sel:WORD_1
	v_pk_fma_f32 v[164:165], v[134:135], v[164:165], v[142:143]
	v_max_f32_e32 v163, 0, v163
	v_max_f32_e32 v165, 0, v165
	v_max_f32_e32 v164, 0, v164
	v_pk_fma_f32 v[166:167], v[136:137], v[166:167], v[144:145]
	v_cvt_pk_f16_f32 v164, v164, v165
	v_max_f32_e32 v165, 0, v167
	v_max_f32_e32 v166, 0, v166
	v_cvt_pk_f16_f32 v163, v168, v163
	v_cvt_pk_f16_f32 v165, v166, v165
	s_waitcnt vmcnt(33)
	v_cvt_f32_f16_e32 v166, v154
	v_cvt_f32_f16_sdwa v167, v154 dst_sel:DWORD dst_unused:UNUSED_PAD src0_sel:WORD_1
	ds_write_b128 v216, v[162:165] offset:4224
	v_cvt_f32_f16_e32 v162, v155
	v_cvt_f32_f16_sdwa v163, v155 dst_sel:DWORD dst_unused:UNUSED_PAD src0_sel:WORD_1
	v_pk_fma_f32 v[164:165], v[130:131], v[166:167], v[138:139]
	v_pk_fma_f32 v[162:163], v[132:133], v[162:163], v[140:141]
	v_max_f32_e32 v166, 0, v165
	v_max_f32_e32 v167, 0, v164
	v_cvt_f32_f16_e32 v164, v156
	v_cvt_f32_f16_sdwa v165, v156 dst_sel:DWORD dst_unused:UNUSED_PAD src0_sel:WORD_1
	v_max_f32_e32 v168, 0, v162
	v_cvt_pk_f16_f32 v162, v167, v166
	v_cvt_f32_f16_e32 v166, v157
	v_cvt_f32_f16_sdwa v167, v157 dst_sel:DWORD dst_unused:UNUSED_PAD src0_sel:WORD_1
	v_pk_fma_f32 v[164:165], v[134:135], v[164:165], v[142:143]
	v_max_f32_e32 v163, 0, v163
	v_max_f32_e32 v165, 0, v165
	v_max_f32_e32 v164, 0, v164
	v_pk_fma_f32 v[166:167], v[136:137], v[166:167], v[144:145]
	v_cvt_pk_f16_f32 v164, v164, v165
	v_max_f32_e32 v165, 0, v167
	v_max_f32_e32 v166, 0, v166
	v_cvt_pk_f16_f32 v163, v168, v163
	v_cvt_pk_f16_f32 v165, v166, v165
	s_waitcnt vmcnt(32)
	v_cvt_f32_f16_e32 v166, v158
	v_cvt_f32_f16_sdwa v167, v158 dst_sel:DWORD dst_unused:UNUSED_PAD src0_sel:WORD_1
	ds_write_b128 v216, v[162:165] offset:8448
	v_cvt_f32_f16_e32 v162, v159
	v_cvt_f32_f16_sdwa v163, v159 dst_sel:DWORD dst_unused:UNUSED_PAD src0_sel:WORD_1
	v_pk_fma_f32 v[164:165], v[130:131], v[166:167], v[138:139]
	v_pk_fma_f32 v[162:163], v[132:133], v[162:163], v[140:141]
	v_max_f32_e32 v166, 0, v165
	v_max_f32_e32 v167, 0, v164
	v_cvt_f32_f16_e32 v164, v160
	v_cvt_f32_f16_sdwa v165, v160 dst_sel:DWORD dst_unused:UNUSED_PAD src0_sel:WORD_1
	v_max_f32_e32 v168, 0, v162
	v_cvt_pk_f16_f32 v162, v167, v166
	v_cvt_f32_f16_e32 v166, v161
	v_cvt_f32_f16_sdwa v167, v161 dst_sel:DWORD dst_unused:UNUSED_PAD src0_sel:WORD_1
	v_pk_fma_f32 v[164:165], v[134:135], v[164:165], v[142:143]
	v_max_f32_e32 v163, 0, v163
	v_max_f32_e32 v165, 0, v165
	v_max_f32_e32 v164, 0, v164
	v_pk_fma_f32 v[166:167], v[136:137], v[166:167], v[144:145]
	v_cvt_pk_f16_f32 v164, v164, v165
	v_max_f32_e32 v165, 0, v167
	v_max_f32_e32 v166, 0, v166
	v_cvt_pk_f16_f32 v163, v168, v163
	v_cvt_pk_f16_f32 v165, v166, v165
	ds_write_b128 v216, v[162:165] offset:12672
	s_waitcnt lgkmcnt(0)
	s_barrier
	s_cbranch_scc1 .LBB3_11
	v_lshrrev_b32_e32 v162, 2, v0
	s_load_dwordx2 s[10:11], s[0:1], 0x10
	s_load_dword s12, s[0:1], 0x50
	s_load_dwordx2 s[8:9], s[0:1], 0x20
	v_and_b32_e32 v181, 12, v162
	s_movk_i32 s13, 0xc0
	v_and_or_b32 v162, v0, s13, v181
	v_lshlrev_b32_e32 v174, 2, v162
	s_waitcnt lgkmcnt(0)
	global_load_dwordx4 v[162:165], v174, s[10:11]
	global_load_dwordx4 v[166:169], v174, s[10:11] offset:64
	global_load_dwordx4 v[170:173], v174, s[10:11] offset:128
	s_nop 0
	global_load_dwordx4 v[174:177], v174, s[10:11] offset:192
	s_load_dwordx2 s[0:1], s[0:1], 0x40
	v_lshlrev_b32_e32 v179, 3, v179
	v_lshlrev_b32_e32 v210, 1, v179
	v_and_b32_e32 v182, 15, v0
	v_lshl_add_u64 v[212:213], s[4:5], 0, v[210:211]
	v_and_b32_e32 v179, 48, v0
	v_mul_u32_u24_e32 v210, 0xc350, v1
	v_lshlrev_b32_e32 v0, 1, v181
	s_waitcnt lgkmcnt(0)
	s_mov_b64 s[18:19], s[0:1]
	s_add_i32 s0, s2, s12
	v_and_b32_e32 v178, 0x300, v178
	v_lshl_or_b32 v218, s0, 5, v180
	s_lshl_b32 s0, s2, 15
	v_lshlrev_b32_e32 v180, 10, v182
	v_or3_b32 v178, s0, v180, v178
	s_movk_i32 s0, 0x40c0
	s_mov_b32 s11, 0x20000
	s_mov_b32 s10, 0x30d4000
	s_and_b32 s9, s9, 0xffff
	s_mov_b32 s13, 0xc350
	v_mad_u32_u24 v217, v182, s7, v179
	s_lshl_b32 s14, s12, 5
	v_add_u32_e32 v219, s6, v182
	v_or3_b32 v220, v178, v179, s0
	s_lshl_b32 s15, s12, 15
	s_mov_b32 s16, 0
	v_add_u32_e32 v210, v210, v219
	s_lshl_b32 s17, s12, 12
	v_lshl_add_u32 v210, v210, 7, v0
	s_waitcnt vmcnt(0)
	s_branch .LBB3_3
